# P4 gate-norm loop software-pipelined (prefetch next iteration loads, double register set) + fused bf16 packs
# speedup vs baseline: 1.0660x; 1.0015x over previous
; __device__ __forceinline__ unsigned pk2(float lo, float hi) { return f2bf(lo) | (f2bf(hi) << 16); }
; __device__ __forceinline__ float siluf_(float x) { return x * __builtin_amdgcn_rcpf(1.0f + __expf(-x)); }
; __device__ __forceinline__ void gdn_gate_norm(const Params& P, size_t wi, size_t nw) {
;     unsigned char* ws = P.ws;
;     bf16* Y = (bf16*)((unsigned char*)P.out + OUT_Y); const v4u* Z = (const v4u*)(ws + WS_Z); const float* SSQG = P.out;
;     for (size_t i = wi; i < (size_t)T * 64; i += nw) {
;         const size_t t = i >> 6; const int c0 = (int)(i & 63) * 8, h = c0 >> 7;
;         const f32x4 q0 = *(const f32x4*)(SSQG + t * 32 + h * 8);
;         const float rstd = rsqrtf(((q0.x + q0.y) + (q0.z + q0.w)) * (1.0f / 128.0f) + 1e-6f);
;         const v4u o = *(const v4u*)(Y + t * 1024 + c0), z = Z[i];
;         const f32x4 w0 = *(const f32x4*)(P.gdn_norm_w + (c0 & 127)), w1 = *(const f32x4*)(P.gdn_norm_w + (c0 & 127) + 4);
;         float y[8];
;         y[0] = bflo(o.x) * rstd * w0.x * siluf_(bflo(z.x)); y[1] = bfhi(o.x) * rstd * w0.y * siluf_(bfhi(z.x));
;         y[2] = bflo(o.y) * rstd * w0.z * siluf_(bflo(z.y)); y[3] = bfhi(o.y) * rstd * w0.w * siluf_(bfhi(z.y));
;         y[4] = bflo(o.z) * rstd * w1.x * siluf_(bflo(z.z)); y[5] = bfhi(o.z) * rstd * w1.y * siluf_(bfhi(z.z));
;         y[6] = bflo(o.w) * rstd * w1.z * siluf_(bflo(z.w)); y[7] = bfhi(o.w) * rstd * w1.w * siluf_(bfhi(z.w));
;         v4u r; r.x = pk2(y[0], y[1]); r.y = pk2(y[2], y[3]); r.z = pk2(y[4], y[5]); r.w = pk2(y[6], y[7]);
;         *(v4u*)(Y + t * 1024 + c0) = r;
;     }
; }
.LBB0_2269:
	s_cmp_lt_i32 s74, 5
	s_cselect_b64 s[4:5], -1, 0
	s_and_b64 s[4:5], s[4:5], s[0:1]
	s_andn2_b64 vcc, exec, s[4:5]
	s_cbranch_vccnz .LBB0_2274
	s_ashr_i32 s3, s2, 31
	s_lshl_b64 s[0:1], s[2:3], 9
	v_or_b32_e32 v2, s0, v0
	v_mov_b32_e32 v3, s1
	s_mov_b64 s[0:1], 0x100000
	v_cmp_gt_u64_e32 vcc, s[0:1], v[2:3]
	s_and_saveexec_b64 s[0:1], vcc
	v_readlane_b32 s8, v254, 4
	v_readlane_b32 s22, v254, 18
	v_readlane_b32 s23, v254, 19
	v_readlane_b32 s9, v254, 5
	v_readlane_b32 s10, v254, 6
	v_readlane_b32 s11, v254, 7
	v_readlane_b32 s12, v254, 8
	v_readlane_b32 s13, v254, 9
	v_readlane_b32 s14, v254, 10
	v_readlane_b32 s15, v254, 11
	v_readlane_b32 s16, v254, 12
	v_readlane_b32 s17, v254, 13
	v_readlane_b32 s18, v254, 14
	v_readlane_b32 s19, v254, 15
	v_readlane_b32 s20, v254, 16
	v_readlane_b32 s21, v254, 17
	s_cbranch_execz .LBB0_2273
	s_ashr_i32 s27, s26, 31
	s_lshl_b64 s[6:7], s[26:27], 9
	s_add_u32 s8, s94, 0x400000
	s_addc_u32 s9, s95, 0
	s_lshl_b64 s[10:11], s[2:3], 13
	s_add_u32 s10, s24, s10
	v_mov_b32_e32 v5, 0
	v_lshlrev_b32_e32 v4, 4, v0
	s_addc_u32 s11, s25, s11
	v_lshl_add_u64 v[6:7], s[10:11], 0, v[4:5]
	s_mov_b64 s[10:11], 0x7c00000
	v_lshlrev_b32_e32 v1, 3, v0
	v_lshl_add_u64 v[6:7], v[6:7], 0, s[10:11]
	s_lshl_b64 s[10:11], s[26:27], 13
	v_lshl_or_b32 v1, s2, 12, v1
	s_lshl_b32 s3, s26, 12
	s_mov_b64 s[12:13], 0
	v_mov_b32_e32 v8, 0x358637bd
	s_mov_b32 s16, 0x800000
	s_mov_b32 s17, 0xffff0000
	s_movk_i32 s18, 0x7fff
	s_mov_b64 s[14:15], 0xfffff
	v_mov_b32_e32 v87, 0
	v_lshrrev_b64 v[14:15], 6, v[2:3]
	global_load_dwordx4 v[10:13], v[6:7], off
	v_lshlrev_b32_e32 v4, 1, v2
	v_lshlrev_b64 v[22:23], 7, v[14:15]
	v_and_b32_e32 v16, 0x78, v1
	v_and_b32_e32 v4, 0x60, v4
	v_lshl_add_u64 v[22:23], s[94:95], 0, v[22:23]
	v_lshlrev_b64 v[24:25], 11, v[14:15]
	v_lshlrev_b32_e32 v26, 2, v16
	v_lshl_add_u64 v[22:23], v[22:23], 0, v[4:5]
	global_load_dwordx4 v[14:17], v26, s[22:23]
	global_load_dwordx4 v[18:21], v26, s[22:23] offset:16
	v_lshl_add_u64 v[26:27], s[8:9], 0, v[24:25]
	global_load_dwordx4 v[22:25], v[22:23], off
	v_and_b32_e32 v9, 0x1f8, v1
	v_lshlrev_b32_e32 v4, 1, v9
	v_lshl_add_u64 v[30:31], v[26:27], 0, v[4:5]
	global_load_dwordx4 v[26:29], v[30:31], off
	v_lshl_add_u64 v[2:3], v[2:3], 0, s[6:7]
	v_cmp_lt_u64_e32 vcc, s[14:15], v[2:3]
	s_or_b64 s[12:13], vcc, s[12:13]
	v_lshl_add_u64 v[6:7], v[6:7], 0, s[10:11]
	v_add_u32_e32 v1, s3, v1
.Lp4_loop:
	s_mov_b64 s[98:99], exec
	s_andn2_b64 exec, exec, s[12:13]
	s_cbranch_execz .Lp4_lastA
	v_lshrrev_b64 v[54:55], 6, v[2:3]
	global_load_dwordx4 v[50:53], v[6:7], off
	v_lshlrev_b32_e32 v86, 1, v2
	v_lshlrev_b64 v[62:63], 7, v[54:55]
	v_and_b32_e32 v56, 0x78, v1
	v_and_b32_e32 v86, 0x60, v86
	v_lshl_add_u64 v[62:63], s[94:95], 0, v[62:63]
	v_lshlrev_b64 v[64:65], 11, v[54:55]
	v_lshlrev_b32_e32 v66, 2, v56
	v_lshl_add_u64 v[62:63], v[62:63], 0, v[86:87]
	global_load_dwordx4 v[54:57], v66, s[22:23]
	global_load_dwordx4 v[58:61], v66, s[22:23] offset:16
	v_lshl_add_u64 v[66:67], s[8:9], 0, v[64:65]
	global_load_dwordx4 v[62:65], v[62:63], off
	v_and_b32_e32 v88, 0x1f8, v1
	v_lshlrev_b32_e32 v86, 1, v88
	v_lshl_add_u64 v[70:71], v[66:67], 0, v[86:87]
	global_load_dwordx4 v[66:69], v[70:71], off
	v_lshl_add_u64 v[2:3], v[2:3], 0, s[6:7]
	v_cmp_lt_u64_e32 vcc, s[14:15], v[2:3]
	s_or_b64 s[12:13], vcc, s[12:13]
	v_lshl_add_u64 v[6:7], v[6:7], 0, s[10:11]
	v_add_u32_e32 v1, s3, v1
	s_mov_b64 s[100:101], exec
	s_mov_b64 exec, s[98:99]
	s_waitcnt vmcnt(5)
	v_lshlrev_b32_e32 v32, 16, v10
	v_mul_f32_e32 v4, 0xbfb8aa3b, v32
	v_exp_f32_e32 v4, v4
	v_lshlrev_b32_e32 v33, 16, v11
	v_lshlrev_b32_e32 v35, 16, v13
	v_lshlrev_b32_e32 v34, 16, v12
	v_and_b32_e32 v13, 0xffff0000, v13
	v_and_b32_e32 v12, 0xffff0000, v12
	v_mov_b32_e32 v36, v14
	v_mov_b32_e32 v37, v16
	v_mov_b32_e32 v16, v15
	v_mov_b32_e32 v14, v18
	v_mov_b32_e32 v15, v20
	v_mov_b32_e32 v20, v19
	v_mov_b32_e32 v18, v23
	v_mov_b32_e32 v19, v24
	v_mov_b32_e32 v23, v25
	v_pk_add_f32 v[18:19], v[18:19], v[22:23]
	v_and_b32_e32 v11, 0xffff0000, v11
	v_add_f32_e32 v18, v18, v19
	v_and_b32_e32 v10, 0xffff0000, v10
	v_mul_f32_e32 v38, 0xbfb8aa3b, v33
	v_mul_f32_e32 v40, 0xbfb8aa3b, v34
	v_mul_f32_e32 v41, 0xbfb8aa3b, v12
	v_mul_f32_e32 v42, 0xbfb8aa3b, v35
	v_mul_f32_e32 v43, 0xbfb8aa3b, v13
	v_add_f32_e32 v4, 1.0, v4
	v_fmamk_f32 v45, v18, 0x3c000000, v8
	v_mul_f32_e32 v9, 0xbfb8aa3b, v10
	v_mul_f32_e32 v39, 0xbfb8aa3b, v11
	v_exp_f32_e32 v38, v38
	v_exp_f32_e32 v40, v40
	v_exp_f32_e32 v41, v41
	v_exp_f32_e32 v42, v42
	v_exp_f32_e32 v43, v43
	v_rcp_f32_e32 v18, v4
	v_mul_f32_e32 v4, 0x4b800000, v45
	v_cmp_gt_f32_e32 vcc, s16, v45
	v_exp_f32_e32 v9, v9
	v_exp_f32_e32 v39, v39
	v_cndmask_b32_e32 v4, v45, v4, vcc
	v_rsq_f32_e32 v4, v4
	v_add_f32_e32 v19, 1.0, v38
	v_add_f32_e32 v40, 1.0, v40
	v_add_f32_e32 v41, 1.0, v41
	v_add_f32_e32 v44, 1.0, v42
	v_add_f32_e32 v43, 1.0, v43
	v_add_f32_e32 v9, 1.0, v9
	v_add_f32_e32 v39, 1.0, v39
	v_rcp_f32_e32 v19, v19
	v_rcp_f32_e32 v40, v40
	v_rcp_f32_e32 v42, v41
	v_rcp_f32_e32 v41, v44
	v_rcp_f32_e32 v43, v43
	v_rcp_f32_e32 v38, v9
	v_rcp_f32_e32 v39, v39
	v_mul_f32_e32 v9, 0x45800000, v4
	v_lshlrev_b32_e32 v23, 16, v27
	v_lshlrev_b32_e32 v22, 16, v26
	v_and_b32_e32 v25, 0xffff0000, v27
	v_and_b32_e32 v24, 0xffff0000, v26
	v_lshlrev_b32_e32 v27, 16, v29
	v_lshlrev_b32_e32 v26, 16, v28
	v_and_b32_e32 v29, 0xffff0000, v29
	v_and_b32_e32 v28, 0xffff0000, v28
	v_cndmask_b32_e32 v4, v4, v9, vcc
	v_pk_mul_f32 v[22:23], v[4:5], v[22:23] op_sel_hi:[0,1]
	v_pk_mul_f32 v[26:27], v[4:5], v[26:27] op_sel_hi:[0,1]
	v_pk_mul_f32 v[28:29], v[4:5], v[28:29] op_sel_hi:[0,1]
	v_pk_mul_f32 v[18:19], v[18:19], v[32:33]
	v_pk_mul_f32 v[32:33], v[40:41], v[34:35]
	v_pk_mul_f32 v[12:13], v[42:43], v[12:13]
	v_pk_mul_f32 v[24:25], v[4:5], v[24:25] op_sel_hi:[0,1]
	v_pk_mul_f32 v[22:23], v[36:37], v[22:23]
	v_pk_mul_f32 v[14:15], v[14:15], v[26:27]
	v_pk_mul_f32 v[20:21], v[20:21], v[28:29]
	v_pk_mul_f32 v[10:11], v[38:39], v[10:11]
	v_pk_mul_f32 v[16:17], v[16:17], v[24:25]
	v_pk_mul_f32 v[18:19], v[18:19], v[22:23]
	v_pk_mul_f32 v[14:15], v[32:33], v[14:15]
	v_pk_mul_f32 v[12:13], v[12:13], v[20:21]
	v_pk_mul_f32 v[10:11], v[10:11], v[16:17]
	v_cvt_pk_bf16_f32 v10, v18, v10
	v_cvt_pk_bf16_f32 v11, v19, v11
	v_cvt_pk_bf16_f32 v12, v14, v12
	v_cvt_pk_bf16_f32 v13, v15, v13
	global_store_dwordx4 v[30:31], v[10:13], off
	s_mov_b64 exec, s[100:101]
	s_mov_b64 s[98:99], exec
	s_andn2_b64 exec, exec, s[12:13]
	s_cbranch_execz .Lp4_lastB
; __device__ __forceinline__ unsigned pk2(float lo, float hi) { return f2bf(lo) | (f2bf(hi) << 16); }
; __device__ __forceinline__ float siluf_(float x) { return x * __builtin_amdgcn_rcpf(1.0f + __expf(-x)); }
; __device__ __forceinline__ void gdn_gate_norm(const Params& P, size_t wi, size_t nw) {
;     unsigned char* ws = P.ws;
;     bf16* Y = (bf16*)((unsigned char*)P.out + OUT_Y); const v4u* Z = (const v4u*)(ws + WS_Z); const float* SSQG = P.out;
;     for (size_t i = wi; i < (size_t)T * 64; i += nw) {
;         const size_t t = i >> 6; const int c0 = (int)(i & 63) * 8, h = c0 >> 7;
;         const f32x4 q0 = *(const f32x4*)(SSQG + t * 32 + h * 8);
;         const float rstd = rsqrtf(((q0.x + q0.y) + (q0.z + q0.w)) * (1.0f / 128.0f) + 1e-6f);
;         const v4u o = *(const v4u*)(Y + t * 1024 + c0), z = Z[i];
;         const f32x4 w0 = *(const f32x4*)(P.gdn_norm_w + (c0 & 127)), w1 = *(const f32x4*)(P.gdn_norm_w + (c0 & 127) + 4);
;         float y[8];
;         y[0] = bflo(o.x) * rstd * w0.x * siluf_(bflo(z.x)); y[1] = bfhi(o.x) * rstd * w0.y * siluf_(bfhi(z.x));
;         y[2] = bflo(o.y) * rstd * w0.z * siluf_(bflo(z.y)); y[3] = bfhi(o.y) * rstd * w0.w * siluf_(bfhi(z.y));
;         y[4] = bflo(o.z) * rstd * w1.x * siluf_(bflo(z.z)); y[5] = bfhi(o.z) * rstd * w1.y * siluf_(bfhi(z.z));
;         y[6] = bflo(o.w) * rstd * w1.z * siluf_(bflo(z.w)); y[7] = bfhi(o.w) * rstd * w1.w * siluf_(bfhi(z.w));
;         v4u r; r.x = pk2(y[0], y[1]); r.y = pk2(y[2], y[3]); r.z = pk2(y[4], y[5]); r.w = pk2(y[6], y[7]);
;         *(v4u*)(Y + t * 1024 + c0) = r;
;     }
; }
	v_lshrrev_b64 v[14:15], 6, v[2:3]
	global_load_dwordx4 v[10:13], v[6:7], off
	v_lshlrev_b32_e32 v4, 1, v2
	v_lshlrev_b64 v[22:23], 7, v[14:15]
	v_and_b32_e32 v16, 0x78, v1
	v_and_b32_e32 v4, 0x60, v4
	v_lshl_add_u64 v[22:23], s[94:95], 0, v[22:23]
	v_lshlrev_b64 v[24:25], 11, v[14:15]
	v_lshlrev_b32_e32 v26, 2, v16
	v_lshl_add_u64 v[22:23], v[22:23], 0, v[4:5]
	global_load_dwordx4 v[14:17], v26, s[22:23]
	global_load_dwordx4 v[18:21], v26, s[22:23] offset:16
	v_lshl_add_u64 v[26:27], s[8:9], 0, v[24:25]
	global_load_dwordx4 v[22:25], v[22:23], off
	v_and_b32_e32 v9, 0x1f8, v1
	v_lshlrev_b32_e32 v4, 1, v9
	v_lshl_add_u64 v[30:31], v[26:27], 0, v[4:5]
	global_load_dwordx4 v[26:29], v[30:31], off
	v_lshl_add_u64 v[2:3], v[2:3], 0, s[6:7]
	v_cmp_lt_u64_e32 vcc, s[14:15], v[2:3]
	s_or_b64 s[12:13], vcc, s[12:13]
	v_lshl_add_u64 v[6:7], v[6:7], 0, s[10:11]
	v_add_u32_e32 v1, s3, v1
	s_mov_b64 s[100:101], exec
	s_mov_b64 exec, s[98:99]
	s_waitcnt vmcnt(5)
	v_lshlrev_b32_e32 v72, 16, v50
	v_mul_f32_e32 v86, 0xbfb8aa3b, v72
	v_exp_f32_e32 v86, v86
	v_lshlrev_b32_e32 v73, 16, v51
	v_lshlrev_b32_e32 v75, 16, v53
	v_lshlrev_b32_e32 v74, 16, v52
	v_and_b32_e32 v53, 0xffff0000, v53
	v_and_b32_e32 v52, 0xffff0000, v52
	v_mov_b32_e32 v76, v54
	v_mov_b32_e32 v77, v56
	v_mov_b32_e32 v56, v55
	v_mov_b32_e32 v54, v58
	v_mov_b32_e32 v55, v60
	v_mov_b32_e32 v60, v59
	v_mov_b32_e32 v58, v63
	v_mov_b32_e32 v59, v64
	v_mov_b32_e32 v63, v65
	v_pk_add_f32 v[58:59], v[58:59], v[62:63]
	v_and_b32_e32 v51, 0xffff0000, v51
	v_add_f32_e32 v58, v58, v59
	v_and_b32_e32 v50, 0xffff0000, v50
	v_mul_f32_e32 v78, 0xbfb8aa3b, v73
	v_mul_f32_e32 v80, 0xbfb8aa3b, v74
	v_mul_f32_e32 v81, 0xbfb8aa3b, v52
	v_mul_f32_e32 v82, 0xbfb8aa3b, v75
	v_mul_f32_e32 v83, 0xbfb8aa3b, v53
	v_add_f32_e32 v86, 1.0, v86
	v_fmamk_f32 v85, v58, 0x3c000000, v8
	v_mul_f32_e32 v88, 0xbfb8aa3b, v50
	v_mul_f32_e32 v79, 0xbfb8aa3b, v51
	v_exp_f32_e32 v78, v78
	v_exp_f32_e32 v80, v80
	v_exp_f32_e32 v81, v81
	v_exp_f32_e32 v82, v82
	v_exp_f32_e32 v83, v83
	v_rcp_f32_e32 v58, v86
	v_mul_f32_e32 v86, 0x4b800000, v85
	v_cmp_gt_f32_e32 vcc, s16, v85
	v_exp_f32_e32 v88, v88
	v_exp_f32_e32 v79, v79
	v_cndmask_b32_e32 v86, v85, v86, vcc
	v_rsq_f32_e32 v86, v86
	v_add_f32_e32 v59, 1.0, v78
	v_add_f32_e32 v80, 1.0, v80
	v_add_f32_e32 v81, 1.0, v81
	v_add_f32_e32 v84, 1.0, v82
	v_add_f32_e32 v83, 1.0, v83
	v_add_f32_e32 v88, 1.0, v88
	v_add_f32_e32 v79, 1.0, v79
	v_rcp_f32_e32 v59, v59
	v_rcp_f32_e32 v80, v80
	v_rcp_f32_e32 v82, v81
	v_rcp_f32_e32 v81, v84
	v_rcp_f32_e32 v83, v83
	v_rcp_f32_e32 v78, v88
	v_rcp_f32_e32 v79, v79
	v_mul_f32_e32 v88, 0x45800000, v86
	v_lshlrev_b32_e32 v63, 16, v67
	v_lshlrev_b32_e32 v62, 16, v66
	v_and_b32_e32 v65, 0xffff0000, v67
	v_and_b32_e32 v64, 0xffff0000, v66
	v_lshlrev_b32_e32 v67, 16, v69
	v_lshlrev_b32_e32 v66, 16, v68
	v_and_b32_e32 v69, 0xffff0000, v69
	v_and_b32_e32 v68, 0xffff0000, v68
	v_cndmask_b32_e32 v86, v86, v88, vcc
	v_pk_mul_f32 v[62:63], v[86:87], v[62:63] op_sel_hi:[0,1]
	v_pk_mul_f32 v[66:67], v[86:87], v[66:67] op_sel_hi:[0,1]
	v_pk_mul_f32 v[68:69], v[86:87], v[68:69] op_sel_hi:[0,1]
	v_pk_mul_f32 v[58:59], v[58:59], v[72:73]
	v_pk_mul_f32 v[72:73], v[80:81], v[74:75]
	v_pk_mul_f32 v[52:53], v[82:83], v[52:53]
	v_pk_mul_f32 v[64:65], v[86:87], v[64:65] op_sel_hi:[0,1]
	v_pk_mul_f32 v[62:63], v[76:77], v[62:63]
	v_pk_mul_f32 v[54:55], v[54:55], v[66:67]
	v_pk_mul_f32 v[60:61], v[60:61], v[68:69]
	v_pk_mul_f32 v[50:51], v[78:79], v[50:51]
	v_pk_mul_f32 v[56:57], v[56:57], v[64:65]
	v_pk_mul_f32 v[58:59], v[58:59], v[62:63]
	v_pk_mul_f32 v[54:55], v[72:73], v[54:55]
	v_pk_mul_f32 v[52:53], v[52:53], v[60:61]
	v_pk_mul_f32 v[50:51], v[50:51], v[56:57]
	v_cvt_pk_bf16_f32 v50, v58, v50
	v_cvt_pk_bf16_f32 v51, v59, v51
	v_cvt_pk_bf16_f32 v52, v54, v52
	v_cvt_pk_bf16_f32 v53, v55, v53
	global_store_dwordx4 v[70:71], v[50:53], off
	s_mov_b64 exec, s[100:101]
	s_branch .Lp4_loop
; __device__ __forceinline__ unsigned pk2(float lo, float hi) { return f2bf(lo) | (f2bf(hi) << 16); }
; __device__ __forceinline__ float siluf_(float x) { return x * __builtin_amdgcn_rcpf(1.0f + __expf(-x)); }
; __device__ __forceinline__ void gdn_gate_norm(const Params& P, size_t wi, size_t nw) {
;     unsigned char* ws = P.ws;
;     bf16* Y = (bf16*)((unsigned char*)P.out + OUT_Y); const v4u* Z = (const v4u*)(ws + WS_Z); const float* SSQG = P.out;
;     for (size_t i = wi; i < (size_t)T * 64; i += nw) {
;         const size_t t = i >> 6; const int c0 = (int)(i & 63) * 8, h = c0 >> 7;
;         const f32x4 q0 = *(const f32x4*)(SSQG + t * 32 + h * 8);
;         const float rstd = rsqrtf(((q0.x + q0.y) + (q0.z + q0.w)) * (1.0f / 128.0f) + 1e-6f);
;         const v4u o = *(const v4u*)(Y + t * 1024 + c0), z = Z[i];
;         const f32x4 w0 = *(const f32x4*)(P.gdn_norm_w + (c0 & 127)), w1 = *(const f32x4*)(P.gdn_norm_w + (c0 & 127) + 4);
;         float y[8];
;         y[0] = bflo(o.x) * rstd * w0.x * siluf_(bflo(z.x)); y[1] = bfhi(o.x) * rstd * w0.y * siluf_(bfhi(z.x));
;         y[2] = bflo(o.y) * rstd * w0.z * siluf_(bflo(z.y)); y[3] = bfhi(o.y) * rstd * w0.w * siluf_(bfhi(z.y));
;         y[4] = bflo(o.z) * rstd * w1.x * siluf_(bflo(z.z)); y[5] = bfhi(o.z) * rstd * w1.y * siluf_(bfhi(z.z));
;         y[6] = bflo(o.w) * rstd * w1.z * siluf_(bflo(z.w)); y[7] = bfhi(o.w) * rstd * w1.w * siluf_(bfhi(z.w));
;         v4u r; r.x = pk2(y[0], y[1]); r.y = pk2(y[2], y[3]); r.z = pk2(y[4], y[5]); r.w = pk2(y[6], y[7]);
;         *(v4u*)(Y + t * 1024 + c0) = r;
;     }
; }
.Lp4_lastA:
	s_mov_b64 exec, s[98:99]
	s_waitcnt vmcnt(0)
	v_lshlrev_b32_e32 v32, 16, v10
	v_mul_f32_e32 v4, 0xbfb8aa3b, v32
	v_exp_f32_e32 v4, v4
	v_lshlrev_b32_e32 v33, 16, v11
	v_lshlrev_b32_e32 v35, 16, v13
	v_lshlrev_b32_e32 v34, 16, v12
	v_and_b32_e32 v13, 0xffff0000, v13
	v_and_b32_e32 v12, 0xffff0000, v12
	v_mov_b32_e32 v36, v14
	v_mov_b32_e32 v37, v16
	v_mov_b32_e32 v16, v15
	v_mov_b32_e32 v14, v18
	v_mov_b32_e32 v15, v20
	v_mov_b32_e32 v20, v19
	v_mov_b32_e32 v18, v23
	v_mov_b32_e32 v19, v24
	v_mov_b32_e32 v23, v25
	v_pk_add_f32 v[18:19], v[18:19], v[22:23]
	v_and_b32_e32 v11, 0xffff0000, v11
	v_add_f32_e32 v18, v18, v19
	v_and_b32_e32 v10, 0xffff0000, v10
	v_mul_f32_e32 v38, 0xbfb8aa3b, v33
	v_mul_f32_e32 v40, 0xbfb8aa3b, v34
	v_mul_f32_e32 v41, 0xbfb8aa3b, v12
	v_mul_f32_e32 v42, 0xbfb8aa3b, v35
	v_mul_f32_e32 v43, 0xbfb8aa3b, v13
	v_add_f32_e32 v4, 1.0, v4
	v_fmamk_f32 v45, v18, 0x3c000000, v8
	v_mul_f32_e32 v9, 0xbfb8aa3b, v10
	v_mul_f32_e32 v39, 0xbfb8aa3b, v11
	v_exp_f32_e32 v38, v38
	v_exp_f32_e32 v40, v40
	v_exp_f32_e32 v41, v41
	v_exp_f32_e32 v42, v42
	v_exp_f32_e32 v43, v43
	v_rcp_f32_e32 v18, v4
	v_mul_f32_e32 v4, 0x4b800000, v45
	v_cmp_gt_f32_e32 vcc, s16, v45
	v_exp_f32_e32 v9, v9
	v_exp_f32_e32 v39, v39
	v_cndmask_b32_e32 v4, v45, v4, vcc
	v_rsq_f32_e32 v4, v4
	v_add_f32_e32 v19, 1.0, v38
	v_add_f32_e32 v40, 1.0, v40
	v_add_f32_e32 v41, 1.0, v41
	v_add_f32_e32 v44, 1.0, v42
	v_add_f32_e32 v43, 1.0, v43
	v_add_f32_e32 v9, 1.0, v9
	v_add_f32_e32 v39, 1.0, v39
	v_rcp_f32_e32 v19, v19
	v_rcp_f32_e32 v40, v40
	v_rcp_f32_e32 v42, v41
	v_rcp_f32_e32 v41, v44
	v_rcp_f32_e32 v43, v43
	v_rcp_f32_e32 v38, v9
	v_rcp_f32_e32 v39, v39
	v_mul_f32_e32 v9, 0x45800000, v4
	v_lshlrev_b32_e32 v23, 16, v27
	v_lshlrev_b32_e32 v22, 16, v26
	v_and_b32_e32 v25, 0xffff0000, v27
	v_and_b32_e32 v24, 0xffff0000, v26
	v_lshlrev_b32_e32 v27, 16, v29
	v_lshlrev_b32_e32 v26, 16, v28
	v_and_b32_e32 v29, 0xffff0000, v29
	v_and_b32_e32 v28, 0xffff0000, v28
	v_cndmask_b32_e32 v4, v4, v9, vcc
	v_pk_mul_f32 v[22:23], v[4:5], v[22:23] op_sel_hi:[0,1]
	v_pk_mul_f32 v[26:27], v[4:5], v[26:27] op_sel_hi:[0,1]
	v_pk_mul_f32 v[28:29], v[4:5], v[28:29] op_sel_hi:[0,1]
	v_pk_mul_f32 v[18:19], v[18:19], v[32:33]
	v_pk_mul_f32 v[32:33], v[40:41], v[34:35]
	v_pk_mul_f32 v[12:13], v[42:43], v[12:13]
	v_pk_mul_f32 v[24:25], v[4:5], v[24:25] op_sel_hi:[0,1]
	v_pk_mul_f32 v[22:23], v[36:37], v[22:23]
	v_pk_mul_f32 v[14:15], v[14:15], v[26:27]
	v_pk_mul_f32 v[20:21], v[20:21], v[28:29]
	v_pk_mul_f32 v[10:11], v[38:39], v[10:11]
	v_pk_mul_f32 v[16:17], v[16:17], v[24:25]
	v_pk_mul_f32 v[18:19], v[18:19], v[22:23]
	v_pk_mul_f32 v[14:15], v[32:33], v[14:15]
	v_pk_mul_f32 v[12:13], v[12:13], v[20:21]
	v_pk_mul_f32 v[10:11], v[10:11], v[16:17]
	v_cvt_pk_bf16_f32 v10, v18, v10
	v_cvt_pk_bf16_f32 v11, v19, v11
	v_cvt_pk_bf16_f32 v12, v14, v12
	v_cvt_pk_bf16_f32 v13, v15, v13
	global_store_dwordx4 v[30:31], v[10:13], off
	s_branch .Lp4_done
.Lp4_lastB:
	s_mov_b64 exec, s[98:99]
	s_waitcnt vmcnt(0)
	v_lshlrev_b32_e32 v72, 16, v50
	v_mul_f32_e32 v86, 0xbfb8aa3b, v72
	v_exp_f32_e32 v86, v86
	v_lshlrev_b32_e32 v73, 16, v51
	v_lshlrev_b32_e32 v75, 16, v53
	v_lshlrev_b32_e32 v74, 16, v52
	v_and_b32_e32 v53, 0xffff0000, v53
	v_and_b32_e32 v52, 0xffff0000, v52
	v_mov_b32_e32 v76, v54
	v_mov_b32_e32 v77, v56
	v_mov_b32_e32 v56, v55
	v_mov_b32_e32 v54, v58
	v_mov_b32_e32 v55, v60
	v_mov_b32_e32 v60, v59
	v_mov_b32_e32 v58, v63
	v_mov_b32_e32 v59, v64
	v_mov_b32_e32 v63, v65
	v_pk_add_f32 v[58:59], v[58:59], v[62:63]
	v_and_b32_e32 v51, 0xffff0000, v51
	v_add_f32_e32 v58, v58, v59
	v_and_b32_e32 v50, 0xffff0000, v50
	v_mul_f32_e32 v78, 0xbfb8aa3b, v73
	v_mul_f32_e32 v80, 0xbfb8aa3b, v74
	v_mul_f32_e32 v81, 0xbfb8aa3b, v52
	v_mul_f32_e32 v82, 0xbfb8aa3b, v75
	v_mul_f32_e32 v83, 0xbfb8aa3b, v53
	v_add_f32_e32 v86, 1.0, v86
	v_fmamk_f32 v85, v58, 0x3c000000, v8
	v_mul_f32_e32 v88, 0xbfb8aa3b, v50
	v_mul_f32_e32 v79, 0xbfb8aa3b, v51
	v_exp_f32_e32 v78, v78
	v_exp_f32_e32 v80, v80
	v_exp_f32_e32 v81, v81
	v_exp_f32_e32 v82, v82
	v_exp_f32_e32 v83, v83
	v_rcp_f32_e32 v58, v86
	v_mul_f32_e32 v86, 0x4b800000, v85
	v_cmp_gt_f32_e32 vcc, s16, v85
	v_exp_f32_e32 v88, v88
	v_exp_f32_e32 v79, v79
	v_cndmask_b32_e32 v86, v85, v86, vcc
	v_rsq_f32_e32 v86, v86
	v_add_f32_e32 v59, 1.0, v78
	v_add_f32_e32 v80, 1.0, v80
	v_add_f32_e32 v81, 1.0, v81
	v_add_f32_e32 v84, 1.0, v82
	v_add_f32_e32 v83, 1.0, v83
	v_add_f32_e32 v88, 1.0, v88
	v_add_f32_e32 v79, 1.0, v79
	v_rcp_f32_e32 v59, v59
	v_rcp_f32_e32 v80, v80
	v_rcp_f32_e32 v82, v81
	v_rcp_f32_e32 v81, v84
	v_rcp_f32_e32 v83, v83
	v_rcp_f32_e32 v78, v88
	v_rcp_f32_e32 v79, v79
	v_mul_f32_e32 v88, 0x45800000, v86
	v_lshlrev_b32_e32 v63, 16, v67
	v_lshlrev_b32_e32 v62, 16, v66
	v_and_b32_e32 v65, 0xffff0000, v67
	v_and_b32_e32 v64, 0xffff0000, v66
	v_lshlrev_b32_e32 v67, 16, v69
	v_lshlrev_b32_e32 v66, 16, v68
	v_and_b32_e32 v69, 0xffff0000, v69
	v_and_b32_e32 v68, 0xffff0000, v68
	v_cndmask_b32_e32 v86, v86, v88, vcc
	v_pk_mul_f32 v[62:63], v[86:87], v[62:63] op_sel_hi:[0,1]
	v_pk_mul_f32 v[66:67], v[86:87], v[66:67] op_sel_hi:[0,1]
	v_pk_mul_f32 v[68:69], v[86:87], v[68:69] op_sel_hi:[0,1]
	v_pk_mul_f32 v[58:59], v[58:59], v[72:73]
	v_pk_mul_f32 v[72:73], v[80:81], v[74:75]
	v_pk_mul_f32 v[52:53], v[82:83], v[52:53]
	v_pk_mul_f32 v[64:65], v[86:87], v[64:65] op_sel_hi:[0,1]
	v_pk_mul_f32 v[62:63], v[76:77], v[62:63]
	v_pk_mul_f32 v[54:55], v[54:55], v[66:67]
	v_pk_mul_f32 v[60:61], v[60:61], v[68:69]
	v_pk_mul_f32 v[50:51], v[78:79], v[50:51]
	v_pk_mul_f32 v[56:57], v[56:57], v[64:65]
	v_pk_mul_f32 v[58:59], v[58:59], v[62:63]
	v_pk_mul_f32 v[54:55], v[72:73], v[54:55]
	v_pk_mul_f32 v[52:53], v[52:53], v[60:61]
	v_pk_mul_f32 v[50:51], v[50:51], v[56:57]
	v_cvt_pk_bf16_f32 v50, v58, v50
	v_cvt_pk_bf16_f32 v51, v59, v51
	v_cvt_pk_bf16_f32 v52, v54, v52
	v_cvt_pk_bf16_f32 v53, v55, v53
	global_store_dwordx4 v[70:71], v[50:53], off
.Lp4_done:
.LBB0_2273:
	s_or_b64 exec, exec, s[0:1]
